# gather-table build in expert GEMM 1 batched (all lookups and token-list loads in flight together); phases H and I reuse the tile tables left in LDS by phase G
# speedup vs baseline: 1.0178x; 1.0056x over previous
.LBB0_1035:
	s_add_i32 s56, s53, 0x22000
	v_cmp_gt_i32_e32 vcc, s18, v243
	s_and_saveexec_b64 s[10:11], vcc
	s_cbranch_execz .LBB0_1044
	s_add_u32 s12, s34, 0x94500000
	s_addc_u32 s13, s35, 0
	s_add_i32 s19, s53, 0x20500
	v_and_b32_e32 v4, 0xff, v243
	v_lshl_add_u32 v5, v243, 2, s56
	s_cmp_eq_u64 s[8:9], 0
	s_cbranch_scc0 .Lgt_general
	s_or_b64 exec, exec, s[10:11]
	v_lshrrev_b32_e32 v97, 8, v243
	v_lshl_add_u32 v97, v97, 5, s54
	v_add_u32_e32 v100, 0, v97
	v_add_u32_e32 v98, s38, v100
	ds_read_u8 v110, v98
	v_add_u32_e32 v101, 64, v97
	v_add_u32_e32 v98, s38, v101
	ds_read_u8 v111, v98
	v_add_u32_e32 v102, 128, v97
	v_add_u32_e32 v98, s38, v102
	ds_read_u8 v112, v98
	v_add_u32_e32 v103, 192, v97
	v_add_u32_e32 v98, s38, v103
	ds_read_u8 v113, v98
	v_add_u32_e32 v104, 256, v97
	v_add_u32_e32 v98, s38, v104
	ds_read_u8 v114, v98
	v_add_u32_e32 v105, 320, v97
	v_add_u32_e32 v98, s38, v105
	ds_read_u8 v115, v98
	v_add_u32_e32 v106, 384, v97
	v_add_u32_e32 v98, s38, v106
	ds_read_u8 v116, v98
	v_add_u32_e32 v107, 448, v97
	v_add_u32_e32 v98, s38, v107
	ds_read_u8 v117, v98
	v_add_u32_e32 v108, 512, v97
	v_add_u32_e32 v98, s38, v108
	ds_read_u8 v118, v98
	s_waitcnt lgkmcnt(0)
	v_lshlrev_b32_e32 v110, 2, v110
	v_add_u32_e32 v98, s3, v110
	ds_read_b32 v120, v98
	v_add_u32_e32 v98, s19, v110
	ds_read_b32 v130, v98
	v_lshlrev_b32_e32 v111, 2, v111
	v_add_u32_e32 v98, s3, v111
	ds_read_b32 v121, v98
	v_add_u32_e32 v98, s19, v111
	ds_read_b32 v131, v98
	v_lshlrev_b32_e32 v112, 2, v112
	v_add_u32_e32 v98, s3, v112
	ds_read_b32 v122, v98
	v_add_u32_e32 v98, s19, v112
	ds_read_b32 v132, v98
	v_lshlrev_b32_e32 v113, 2, v113
	v_add_u32_e32 v98, s3, v113
	ds_read_b32 v123, v98
	v_add_u32_e32 v98, s19, v113
	ds_read_b32 v133, v98
	v_lshlrev_b32_e32 v114, 2, v114
	v_add_u32_e32 v98, s3, v114
	ds_read_b32 v124, v98
	v_add_u32_e32 v98, s19, v114
	ds_read_b32 v134, v98
	v_lshlrev_b32_e32 v115, 2, v115
	v_add_u32_e32 v98, s3, v115
	ds_read_b32 v125, v98
	v_add_u32_e32 v98, s19, v115
	ds_read_b32 v135, v98
	v_lshlrev_b32_e32 v116, 2, v116
	v_add_u32_e32 v98, s3, v116
	ds_read_b32 v126, v98
	v_add_u32_e32 v98, s19, v116
	ds_read_b32 v136, v98
	v_lshlrev_b32_e32 v117, 2, v117
	v_add_u32_e32 v98, s3, v117
	ds_read_b32 v127, v98
	v_add_u32_e32 v98, s19, v117
	ds_read_b32 v137, v98
	v_lshlrev_b32_e32 v118, 2, v118
	v_add_u32_e32 v98, s3, v118
	ds_read_b32 v128, v98
	v_add_u32_e32 v98, s19, v118
	ds_read_b32 v138, v98
	s_waitcnt lgkmcnt(0)
	v_sub_u32_e32 v100, v100, v120
	v_lshl_or_b32 v100, v100, 8, v4
	v_add_u32_e32 v98, 0, v243
	v_cmp_gt_i32_e64 s[60:61], s18, v98
	v_cmp_lt_i32_e64 s[62:63], v100, v130
	s_and_b64 vcc, s[60:61], s[62:63]
	v_lshlrev_b32_e32 v110, 15, v110
	v_lshl_add_u32 v110, v100, 2, v110
	v_cndmask_b32_e32 v110, 0, v110, vcc
	v_cndmask_b32_e64 v120, 0, -1, vcc
	global_load_dword v140, v110, s[12:13]
	v_sub_u32_e32 v101, v101, v121
	v_lshl_or_b32 v101, v101, 8, v4
	v_add_u32_e32 v98, 512, v243
	v_cmp_gt_i32_e64 s[60:61], s18, v98
	v_cmp_lt_i32_e64 s[62:63], v101, v131
	s_and_b64 vcc, s[60:61], s[62:63]
	v_lshlrev_b32_e32 v111, 15, v111
	v_lshl_add_u32 v111, v101, 2, v111
	v_cndmask_b32_e32 v111, 0, v111, vcc
	v_cndmask_b32_e64 v121, 0, -1, vcc
	global_load_dword v141, v111, s[12:13]
	v_sub_u32_e32 v102, v102, v122
	v_lshl_or_b32 v102, v102, 8, v4
	v_add_u32_e32 v98, 1024, v243
	v_cmp_gt_i32_e64 s[60:61], s18, v98
	v_cmp_lt_i32_e64 s[62:63], v102, v132
	s_and_b64 vcc, s[60:61], s[62:63]
	v_lshlrev_b32_e32 v112, 15, v112
	v_lshl_add_u32 v112, v102, 2, v112
	v_cndmask_b32_e32 v112, 0, v112, vcc
	v_cndmask_b32_e64 v122, 0, -1, vcc
	global_load_dword v142, v112, s[12:13]
	v_sub_u32_e32 v103, v103, v123
	v_lshl_or_b32 v103, v103, 8, v4
	v_add_u32_e32 v98, 1536, v243
	v_cmp_gt_i32_e64 s[60:61], s18, v98
	v_cmp_lt_i32_e64 s[62:63], v103, v133
	s_and_b64 vcc, s[60:61], s[62:63]
	v_lshlrev_b32_e32 v113, 15, v113
	v_lshl_add_u32 v113, v103, 2, v113
	v_cndmask_b32_e32 v113, 0, v113, vcc
	v_cndmask_b32_e64 v123, 0, -1, vcc
	global_load_dword v143, v113, s[12:13]
	v_sub_u32_e32 v104, v104, v124
	v_lshl_or_b32 v104, v104, 8, v4
	v_add_u32_e32 v98, 2048, v243
	v_cmp_gt_i32_e64 s[60:61], s18, v98
	v_cmp_lt_i32_e64 s[62:63], v104, v134
	s_and_b64 vcc, s[60:61], s[62:63]
	v_lshlrev_b32_e32 v114, 15, v114
	v_lshl_add_u32 v114, v104, 2, v114
	v_cndmask_b32_e32 v114, 0, v114, vcc
	v_cndmask_b32_e64 v124, 0, -1, vcc
	global_load_dword v144, v114, s[12:13]
	v_sub_u32_e32 v105, v105, v125
	v_lshl_or_b32 v105, v105, 8, v4
	v_add_u32_e32 v98, 2560, v243
	v_cmp_gt_i32_e64 s[60:61], s18, v98
	v_cmp_lt_i32_e64 s[62:63], v105, v135
	s_and_b64 vcc, s[60:61], s[62:63]
	v_lshlrev_b32_e32 v115, 15, v115
	v_lshl_add_u32 v115, v105, 2, v115
	v_cndmask_b32_e32 v115, 0, v115, vcc
	v_cndmask_b32_e64 v125, 0, -1, vcc
	global_load_dword v145, v115, s[12:13]
	v_sub_u32_e32 v106, v106, v126
	v_lshl_or_b32 v106, v106, 8, v4
	v_add_u32_e32 v98, 3072, v243
	v_cmp_gt_i32_e64 s[60:61], s18, v98
	v_cmp_lt_i32_e64 s[62:63], v106, v136
	s_and_b64 vcc, s[60:61], s[62:63]
	v_lshlrev_b32_e32 v116, 15, v116
	v_lshl_add_u32 v116, v106, 2, v116
	v_cndmask_b32_e32 v116, 0, v116, vcc
	v_cndmask_b32_e64 v126, 0, -1, vcc
	global_load_dword v146, v116, s[12:13]
	v_sub_u32_e32 v107, v107, v127
	v_lshl_or_b32 v107, v107, 8, v4
	v_add_u32_e32 v98, 3584, v243
	v_cmp_gt_i32_e64 s[60:61], s18, v98
	v_cmp_lt_i32_e64 s[62:63], v107, v137
	s_and_b64 vcc, s[60:61], s[62:63]
	v_lshlrev_b32_e32 v117, 15, v117
	v_lshl_add_u32 v117, v107, 2, v117
	v_cndmask_b32_e32 v117, 0, v117, vcc
	v_cndmask_b32_e64 v127, 0, -1, vcc
	global_load_dword v147, v117, s[12:13]
	v_sub_u32_e32 v108, v108, v128
	v_lshl_or_b32 v108, v108, 8, v4
	v_add_u32_e32 v98, 4096, v243
	v_cmp_gt_i32_e64 s[60:61], s18, v98
	v_cmp_lt_i32_e64 s[62:63], v108, v138
	s_and_b64 vcc, s[60:61], s[62:63]
	v_lshlrev_b32_e32 v118, 15, v118
	v_lshl_add_u32 v118, v108, 2, v118
	v_cndmask_b32_e32 v118, 0, v118, vcc
	v_cndmask_b32_e64 v128, 0, -1, vcc
	global_load_dword v148, v118, s[12:13]
	s_waitcnt vmcnt(8)
	v_lshlrev_b32_e32 v140, 10, v140
	v_and_b32_e32 v140, v140, v120
	ds_write_b32 v5, v140
	s_waitcnt vmcnt(7)
	v_lshlrev_b32_e32 v141, 10, v141
	v_and_b32_e32 v141, v141, v121
	ds_write_b32 v5, v141 offset:2048
	s_waitcnt vmcnt(6)
	v_lshlrev_b32_e32 v142, 10, v142
	v_and_b32_e32 v142, v142, v122
	ds_write_b32 v5, v142 offset:4096
	s_waitcnt vmcnt(5)
	v_lshlrev_b32_e32 v143, 10, v143
	v_and_b32_e32 v143, v143, v123
	ds_write_b32 v5, v143 offset:6144
	s_waitcnt vmcnt(4)
	v_lshlrev_b32_e32 v144, 10, v144
	v_and_b32_e32 v144, v144, v124
	ds_write_b32 v5, v144 offset:8192
	s_waitcnt vmcnt(3)
	v_lshlrev_b32_e32 v145, 10, v145
	v_and_b32_e32 v145, v145, v125
	ds_write_b32 v5, v145 offset:10240
	s_waitcnt vmcnt(2)
	v_lshlrev_b32_e32 v146, 10, v146
	v_and_b32_e32 v146, v146, v126
	ds_write_b32 v5, v146 offset:12288
	s_waitcnt vmcnt(1)
	v_lshlrev_b32_e32 v147, 10, v147
	v_and_b32_e32 v147, v147, v127
	ds_write_b32 v5, v147 offset:14336
	s_waitcnt vmcnt(0)
	v_lshlrev_b32_e32 v148, 10, v148
	v_and_b32_e32 v148, v148, v128
	ds_write_b32 v5, v148 offset:16384
	s_branch .LBB0_1044
.Lgt_general:
	s_mov_b64 s[14:15], 0
	v_mov_b32_e32 v6, v243
	s_branch .LBB0_1038

.LBB0_1125:
	s_andn2_b64 vcc, exec, s[4:5]
	s_cbranch_vccnz .LBB0_1216
	s_add_i32 s3, s53, 0x20180
	v_mov_b32_e32 v2, s3
	s_waitcnt vmcnt(0) lgkmcnt(0)
	ds_read_b32 v2, v2
	s_add_i32 s39, s53, 0x20200
	s_waitcnt lgkmcnt(0)
	v_readfirstlane_b32 s45, v2
	s_branch .Lh_tiles_done
	s_waitcnt vmcnt(0)
	v_and_b32_e32 v2, 63, v182
	v_cmp_gt_u32_e64 s[4:5], 32, v2
	v_mov_b32_e32 v3, 0
	s_and_saveexec_b64 s[6:7], s[4:5]
	s_cbranch_execz .LBB0_1129
	s_lshl_b32 s40, s74, 6
	s_lshl_b64 s[8:9], s[40:41], 2
	s_add_u32 s8, s30, s8
	v_and_b32_e32 v3, 31, v182
	s_addc_u32 s9, s31, s9
	v_lshlrev_b32_e32 v214, 2, v3
	v_lshl_add_u64 v[4:5], s[8:9], 0, v[214:215]
	v_add_co_u32_e32 v4, vcc, 0x10000, v4
	s_nop 1
	v_addc_co_u32_e32 v5, vcc, 0, v5, vcc
	global_load_dword v3, v[4:5], off sc1

.Lh_tiles_done:
	s_load_dwordx2 s[4:5], s[0:1], 0x80
	s_cmpk_lg_i32 s29, 0x100
	s_cselect_b64 s[6:7], -1, 0
	v_readfirstlane_b32 s12, v182
	s_mov_b64 s[10:11], -1
	s_and_b64 vcc, exec, s[6:7]
	s_cbranch_vccnz .LBB0_1140
	s_andn2_b64 vcc, exec, s[10:11]
	s_cbranch_vccz .LBB0_1141

.LBB0_1216:
	s_cmp_gt_i32 s58, s26
	s_cselect_b64 s[6:7], -1, 0
	s_cmp_ge_i32 s26, s65
	s_cselect_b64 s[8:9], -1, 0
	s_waitcnt vmcnt(0)
	v_mov_b32_e32 v3, v0
	s_or_b64 s[6:7], s[6:7], s[8:9]
	s_mov_b32 s3, s2
	s_waitcnt lgkmcnt(0)
	v_readfirstlane_b32 s4, v3
	s_mov_b32 s24, s73
	s_and_b64 vcc, exec, s[6:7]
	s_cbranch_vccnz .LBB0_217
	s_ashr_i32 s29, s4, 6
	v_and_b32_e32 v2, 63, v3
	s_load_dwordx2 s[6:7], s[0:1], 0xa0
	s_add_i32 s38, s53, 0x20100
	s_waitcnt vmcnt(0) lgkmcnt(0)
	s_branch .Li_tiles_done
	v_cmp_gt_i32_e64 s[4:5], 32, v2
	v_mov_b32_e32 v4, 0
	s_and_saveexec_b64 s[8:9], s[4:5]
	s_cbranch_execz .LBB0_1220
	s_lshl_b32 s40, s74, 6
	s_lshl_b64 s[10:11], s[40:41], 2
	s_add_u32 s10, s30, s10
	v_and_b32_e32 v4, 31, v2
	s_addc_u32 s11, s31, s11
	v_lshlrev_b32_e32 v214, 2, v4
	v_lshl_add_u64 v[4:5], s[10:11], 0, v[214:215]
	v_add_co_u32_e32 v4, vcc, 0x10000, v4
	s_nop 1
	v_addc_co_u32_e32 v5, vcc, 0, v5, vcc
	global_load_dword v4, v[4:5], off sc1

.Li_tiles_done:
	s_load_dwordx2 s[12:13], s[0:1], 0x48
	s_load_dwordx2 s[10:11], s[0:1], 0x50
	s_load_dwordx2 s[14:15], s[0:1], 0x88
	s_load_dwordx2 s[18:19], s[0:1], 0x90
	s_load_dwordx2 s[8:9], s[0:1], 0x98
	s_lshl_b32 s39, s3, 3
	s_add_i32 s4, s29, s39
	s_cmpk_gt_i32 s4, 0x7fff
	s_cbranch_scc1 .LBB0_1281
	s_add_u32 s45, s6, 0x5d200000
	s_addc_u32 s54, s7, 0
	s_lshl_b32 s40, s74, 10
	s_lshl_b64 s[16:17], s[40:41], 2
	v_lshlrev_b32_e32 v30, 2, v2
	s_waitcnt lgkmcnt(0)
	s_add_u32 s12, s12, s16
	v_ashrrev_i32_e32 v31, 31, v30
	s_addc_u32 s13, s13, s17
	v_lshlrev_b64 v[14:15], 2, v[30:31]
	v_lshl_add_u64 v[6:7], s[12:13], 0, v[14:15]
	global_load_dwordx4 v[2:5], v[6:7], off
	s_add_u32 s10, s10, s16
	s_addc_u32 s11, s11, s17
	v_lshl_add_u64 v[8:9], s[10:11], 0, v[14:15]
	s_add_u32 s10, s6, 0x83200000
	s_addc_u32 s11, s7, 0
	s_add_u32 s40, s6, 0x94200000
	s_addc_u32 s56, s7, 0
	s_add_u32 s57, s6, 0x94300000
	s_addc_u32 s75, s7, 0
	s_add_u32 s80, s6, 0x94400000
	s_addc_u32 s81, s7, 0
	s_lshl_b32 s5, s24, 3
	s_add_u32 s82, s6, 0x3a200000
	s_addc_u32 s83, s7, 0
	s_lshl_b32 s59, s24, 4
	s_add_u32 s12, s6, 0x4d200000
	s_addc_u32 s13, s7, 0
	s_add_i32 s5, s4, s5
	s_min_i32 s20, s5, 0x7fff
	s_ashr_i32 s21, s20, 31
	s_lshl_b64 s[22:23], s[20:21], 11
	s_add_u32 s22, s12, s22
	s_addc_u32 s23, s13, s23
	v_lshlrev_b64 v[16:17], 1, v[30:31]
	v_lshl_add_u64 v[78:79], s[12:13], 0, v[16:17]
	s_mul_i32 s89, s24, 40
	s_waitcnt vmcnt(0)
	v_pk_mul_f32 v[32:33], v[4:5], s[66:67] op_sel_hi:[1,0]
	v_pk_mul_f32 v[34:35], v[2:3], s[66:67] op_sel_hi:[1,0]
	global_load_dwordx4 v[2:5], v[8:9], off
	s_waitcnt vmcnt(0)
	v_pk_mul_f32 v[36:37], v[4:5], s[66:67] op_sel_hi:[1,0]
	v_pk_mul_f32 v[38:39], v[2:3], s[66:67] op_sel_hi:[1,0]
	global_load_dwordx4 v[2:5], v[6:7], off offset:1024
	s_waitcnt vmcnt(0)
	v_pk_mul_f32 v[40:41], v[4:5], s[66:67] op_sel_hi:[1,0]
	v_pk_mul_f32 v[42:43], v[2:3], s[66:67] op_sel_hi:[1,0]
	global_load_dwordx4 v[2:5], v[8:9], off offset:1024
	s_waitcnt vmcnt(0)
	v_pk_mul_f32 v[44:45], v[4:5], s[66:67] op_sel_hi:[1,0]
	v_pk_mul_f32 v[46:47], v[2:3], s[66:67] op_sel_hi:[1,0]
	global_load_dwordx4 v[2:5], v[6:7], off offset:2048
	s_waitcnt vmcnt(0)
	v_pk_mul_f32 v[48:49], v[4:5], s[66:67] op_sel_hi:[1,0]
	v_pk_mul_f32 v[50:51], v[2:3], s[66:67] op_sel_hi:[1,0]
	global_load_dwordx4 v[2:5], v[8:9], off offset:2048
	s_waitcnt vmcnt(0)
	v_pk_mul_f32 v[52:53], v[4:5], s[66:67] op_sel_hi:[1,0]
	v_pk_mul_f32 v[54:55], v[2:3], s[66:67] op_sel_hi:[1,0]
	global_load_dwordx4 v[2:5], v[6:7], off offset:3072
	s_waitcnt vmcnt(0)
	v_pk_mul_f32 v[56:57], v[4:5], s[66:67] op_sel_hi:[1,0]
	v_pk_mul_f32 v[58:59], v[2:3], s[66:67] op_sel_hi:[1,0]
	global_load_dwordx4 v[2:5], v[8:9], off offset:3072
	s_waitcnt vmcnt(0)
	v_pk_mul_f32 v[62:63], v[2:3], s[66:67] op_sel_hi:[1,0]
	v_lshl_add_u64 v[2:3], s[22:23], 0, v[16:17]
	s_lshl_b64 s[22:23], s[20:21], 3
	s_add_u32 s22, s45, s22
	s_addc_u32 s23, s54, s23
	s_lshl_b32 s20, s20, 2
	s_ashr_i32 s21, s20, 31
	s_lshl_b64 s[20:21], s[20:21], 2
	global_load_dwordx2 v[64:65], v[2:3], off offset:1536
	global_load_dwordx2 v[72:73], v[2:3], off offset:1024
	global_load_dwordx2 v[74:75], v[2:3], off offset:512
	global_load_dwordx2 v[76:77], v[2:3], off
	global_load_dwordx2 v[70:71], v215, s[22:23]
	s_add_u32 s22, s40, s20
	s_addc_u32 s23, s56, s21
	v_pk_mul_f32 v[60:61], v[4:5], s[66:67] op_sel_hi:[1,0]
	global_load_dwordx4 v[2:5], v215, s[22:23]
	s_add_u32 s22, s80, s20
	s_addc_u32 s23, s81, s21
	s_add_u32 s20, s57, s20
	s_addc_u32 s21, s75, s21
	s_add_u32 s18, s18, s16
	s_addc_u32 s19, s19, s17
	s_ashr_i32 s5, s4, 31
	v_lshl_add_u64 v[82:83], s[18:19], 0, v[14:15]
	s_waitcnt vmcnt(0)
	v_lshlrev_b32_e32 v5, 2, v5
	v_add_u32_e32 v5, s38, v5
	ds_read_b32 v6, v5
	v_lshlrev_b32_e32 v4, 2, v4
	v_add_u32_e32 v4, s38, v4
	v_lshlrev_b32_e32 v3, 2, v3
	v_add_u32_e32 v3, s38, v3
	s_waitcnt lgkmcnt(0)
	v_ashrrev_i32_e32 v7, 31, v6
	v_lshlrev_b64 v[6:7], 18, v[6:7]
	v_lshl_add_u64 v[10:11], s[10:11], 0, v[6:7]
	global_load_dwordx4 v[6:9], v215, s[22:23]
	v_lshlrev_b32_e32 v2, 2, v2
	v_add_u32_e32 v2, s38, v2
	s_lshl_b64 s[22:23], s[4:5], 11
	s_waitcnt vmcnt(0)
	v_mov_b32_e32 v214, v9
	v_lshlrev_b64 v[12:13], 10, v[214:215]
	v_lshl_add_u64 v[10:11], v[10:11], 0, v[12:13]
	v_lshl_add_u64 v[10:11], v[10:11], 0, v[30:31]
	global_load_dword v122, v[10:11], off offset:768
	global_load_dword v123, v[10:11], off offset:512
	global_load_dword v124, v[10:11], off offset:256
	global_load_dword v125, v[10:11], off
	ds_read_b32 v4, v4
	v_mov_b32_e32 v9, v215
	v_lshlrev_b64 v[8:9], 10, v[8:9]
	v_mov_b32_e32 v214, v7
	v_mov_b32_e32 v7, v215
	s_waitcnt lgkmcnt(0)
	v_ashrrev_i32_e32 v5, 31, v4
	v_lshlrev_b64 v[4:5], 18, v[4:5]
	v_lshl_add_u64 v[4:5], s[10:11], 0, v[4:5]
	v_lshl_add_u64 v[4:5], v[4:5], 0, v[8:9]
	v_lshl_add_u64 v[4:5], v[4:5], 0, v[30:31]
	global_load_dword v118, v[4:5], off offset:768
	global_load_dword v119, v[4:5], off offset:512
	global_load_dword v120, v[4:5], off offset:256
	global_load_dword v121, v[4:5], off
	ds_read_b32 v4, v3
	v_lshlrev_b64 v[8:9], 10, v[214:215]
	s_waitcnt lgkmcnt(0)
	v_ashrrev_i32_e32 v5, 31, v4
	v_lshlrev_b64 v[4:5], 18, v[4:5]
	v_lshl_add_u64 v[4:5], s[10:11], 0, v[4:5]
	v_lshl_add_u64 v[4:5], v[4:5], 0, v[8:9]
	v_lshl_add_u64 v[4:5], v[4:5], 0, v[30:31]
	global_load_dword v114, v[4:5], off offset:768
	global_load_dword v115, v[4:5], off offset:512
	global_load_dword v116, v[4:5], off offset:256
	global_load_dword v117, v[4:5], off
	ds_read_b32 v2, v2
	v_lshlrev_b64 v[4:5], 10, v[6:7]
	s_waitcnt lgkmcnt(0)
	v_ashrrev_i32_e32 v3, 31, v2
	v_lshlrev_b64 v[2:3], 18, v[2:3]
	v_lshl_add_u64 v[2:3], s[10:11], 0, v[2:3]
	v_lshl_add_u64 v[2:3], v[2:3], 0, v[4:5]
	v_lshl_add_u64 v[2:3], v[2:3], 0, v[30:31]
	global_load_dword v110, v[2:3], off offset:768
	global_load_dword v111, v[2:3], off offset:512
	global_load_dword v112, v[2:3], off offset:256
	global_load_dword v113, v[2:3], off
	global_load_dwordx4 v[10:13], v215, s[20:21]
	s_add_u32 s20, s12, s22
	s_addc_u32 s21, s13, s23
	v_lshl_add_u64 v[2:3], s[20:21], 0, v[16:17]
	s_lshl_b64 s[20:21], s[4:5], 3
	s_add_u32 s20, s45, s20
	s_addc_u32 s21, s54, s21
	global_load_dwordx2 v[84:85], v[2:3], off offset:1536
	global_load_dwordx2 v[88:89], v[2:3], off offset:1024
	global_load_dwordx2 v[90:91], v[2:3], off offset:512
	global_load_dwordx2 v[92:93], v[2:3], off
	global_load_dwordx2 v[86:87], v215, s[20:21]
	s_add_u32 s20, s14, s16
	s_addc_u32 s21, s15, s17
	s_lshl_b32 s14, s4, 2
	s_ashr_i32 s15, s14, 31
	s_lshl_b64 s[14:15], s[14:15], 2
	s_add_u32 s16, s40, s14
	s_addc_u32 s17, s56, s15
	global_load_dwordx4 v[2:5], v215, s[16:17]
	s_add_u32 s16, s80, s14
	s_addc_u32 s17, s81, s15
	s_add_u32 s14, s57, s14
	s_addc_u32 s15, s75, s15
	v_and_b32_e32 v16, 64, v233
	v_add_u32_e32 v16, 64, v16
	v_xor_b32_e32 v17, 1, v233
	v_cmp_lt_i32_e32 vcc, v17, v16
	s_mul_i32 s12, s24, 24
	v_lshl_add_u64 v[80:81], s[20:21], 0, v[14:15]
	v_cndmask_b32_e32 v17, v233, v17, vcc
	v_lshlrev_b32_e32 v126, 2, v17
	v_xor_b32_e32 v17, 2, v233
	v_cmp_lt_i32_e32 vcc, v17, v16
	s_waitcnt vmcnt(0)
	v_lshlrev_b32_e32 v5, 2, v5
	v_add_u32_e32 v5, s38, v5
	ds_read_b32 v6, v5
	v_lshlrev_b32_e32 v4, 2, v4
	v_add_u32_e32 v4, s38, v4
	v_lshlrev_b32_e32 v3, 2, v3
	v_add_u32_e32 v3, s38, v3
	s_waitcnt lgkmcnt(0)
	v_ashrrev_i32_e32 v7, 31, v6
	v_lshlrev_b64 v[6:7], 18, v[6:7]
	v_lshl_add_u64 v[18:19], s[10:11], 0, v[6:7]
	global_load_dwordx4 v[6:9], v215, s[16:17]
	v_lshlrev_b32_e32 v2, 2, v2
	v_add_u32_e32 v2, s38, v2
	v_cndmask_b32_e32 v17, v233, v17, vcc
	v_lshlrev_b32_e32 v127, 2, v17
	v_xor_b32_e32 v17, 4, v233
	v_cmp_lt_i32_e32 vcc, v17, v16
	s_waitcnt vmcnt(0)
	v_mov_b32_e32 v214, v9
	v_lshlrev_b64 v[20:21], 10, v[214:215]
	v_lshl_add_u64 v[18:19], v[18:19], 0, v[20:21]
	v_lshl_add_u64 v[18:19], v[18:19], 0, v[30:31]
	global_load_dword v132, v[18:19], off offset:768
	global_load_dword v133, v[18:19], off offset:512
	global_load_dword v134, v[18:19], off offset:256
	global_load_dword v135, v[18:19], off
	ds_read_b32 v4, v4
	v_mov_b32_e32 v9, v215
	v_lshlrev_b64 v[8:9], 10, v[8:9]
	v_mov_b32_e32 v214, v7
	v_mov_b32_e32 v7, v215
	s_waitcnt lgkmcnt(0)
	v_ashrrev_i32_e32 v5, 31, v4
	v_lshlrev_b64 v[4:5], 18, v[4:5]
	v_lshl_add_u64 v[4:5], s[10:11], 0, v[4:5]
	v_lshl_add_u64 v[4:5], v[4:5], 0, v[8:9]
	v_lshl_add_u64 v[4:5], v[4:5], 0, v[30:31]
	global_load_dword v144, v[4:5], off offset:768
	global_load_dword v145, v[4:5], off offset:512
	global_load_dword v146, v[4:5], off offset:256
	global_load_dword v147, v[4:5], off
	ds_read_b32 v4, v3
	v_lshlrev_b64 v[8:9], 10, v[214:215]
	v_cndmask_b32_e32 v17, v233, v17, vcc
	v_lshlrev_b32_e32 v128, 2, v17
	v_xor_b32_e32 v17, 8, v233
	s_waitcnt lgkmcnt(0)
	v_ashrrev_i32_e32 v5, 31, v4
	v_lshlrev_b64 v[4:5], 18, v[4:5]
	v_lshl_add_u64 v[4:5], s[10:11], 0, v[4:5]
	v_lshl_add_u64 v[4:5], v[4:5], 0, v[8:9]
	v_lshl_add_u64 v[4:5], v[4:5], 0, v[30:31]
	global_load_dword v140, v[4:5], off offset:768
	global_load_dword v141, v[4:5], off offset:512
	global_load_dword v142, v[4:5], off offset:256
	global_load_dword v143, v[4:5], off
	ds_read_b32 v2, v2
	v_lshlrev_b64 v[4:5], 10, v[6:7]
	v_cmp_lt_i32_e32 vcc, v17, v16
	s_waitcnt lgkmcnt(0)
	v_ashrrev_i32_e32 v3, 31, v2
	v_lshlrev_b64 v[2:3], 18, v[2:3]
	v_lshl_add_u64 v[2:3], s[10:11], 0, v[2:3]
	v_lshl_add_u64 v[2:3], v[2:3], 0, v[4:5]
	v_lshl_add_u64 v[2:3], v[2:3], 0, v[30:31]
	global_load_dword v136, v[2:3], off offset:768
	global_load_dword v137, v[2:3], off offset:512
	global_load_dword v138, v[2:3], off offset:256
	global_load_dword v139, v[2:3], off
	v_cndmask_b32_e32 v17, v233, v17, vcc
	global_load_dwordx4 v[2:5], v215, s[14:15]
	s_add_i32 s14, s4, s59
	s_min_i32 s14, s14, 0x7fff
	s_lshl_b32 s14, s14, 2
	s_ashr_i32 s15, s14, 31
	s_lshl_b64 s[14:15], s[14:15], 2
	s_add_u32 s16, s57, s14
	s_addc_u32 s17, s75, s15
	global_load_dwordx4 v[6:9], v215, s[16:17]
	s_add_u32 s16, s80, s14
	s_addc_u32 s17, s81, s15
	s_add_u32 s14, s40, s14
	s_addc_u32 s15, s56, s15
	global_load_dwordx4 v[18:21], v215, s[16:17]
	global_load_dwordx4 v[22:25], v215, s[14:15]
	s_cmp_eq_u32 s74, 3
	s_cselect_b64 s[14:15], -1, 0
	s_cmp_lg_u32 s74, 3
	s_cselect_b64 s[16:17], -1, 0
	s_add_u32 s84, s6, 0x32200000
	s_addc_u32 s85, s7, 0
	s_lshl_b32 s60, s24, 5
	s_add_i32 s24, s24, s3
	s_add_i32 s89, s89, s39
	s_lshl_b32 s97, s24, 3
	s_add_i32 s60, s60, s39
	s_lshl_b64 s[6:7], s[4:5], 10
	v_lshlrev_b32_e32 v129, 2, v17
	v_xor_b32_e32 v17, 16, v233
	s_add_u32 s61, s84, s6
	v_cmp_lt_i32_e32 vcc, v17, v16
	s_addc_u32 s65, s85, s7
	s_ashr_i32 s13, s12, 31
	v_cndmask_b32_e32 v17, v233, v17, vcc
	s_lshl_b64 s[18:19], s[12:13], 10
	s_lshl_b64 s[4:5], s[4:5], 12
	v_lshlrev_b32_e32 v130, 2, v17
	v_xor_b32_e32 v17, 32, v233
	s_add_u32 s62, s8, s4
	v_cmp_lt_i32_e32 vcc, v17, v16
	s_addc_u32 s63, s9, s5
	s_lshl_b64 s[20:21], s[12:13], 12
	v_cndmask_b32_e32 v16, v233, v17, vcc
	s_add_u32 s33, s82, s22
	v_lshlrev_b32_e32 v131, 2, v16
	s_addc_u32 s3, s83, s23
	s_lshl_b64 s[22:23], s[12:13], 11
	s_add_i32 s13, s12, s39
	s_add_i32 s59, s59, s39
	s_branch .LBB0_1230
